# baseline (speedup 1.0000x reference)
_Z9ln_kernelILi2EEvPKiPKfS3_PfS3_S3_PDF16_:
	s_load_dwordx4 s[12:15], s[0:1], 0x20
	v_and_b32_e32 v62, 63, v0
	v_lshlrev_b32_e32 v62, 4, v62
	s_load_dwordx8 s[4:11], s[0:1], 0x8
	v_and_b32_e32 v12, 63, v0
	v_lshrrev_b32_e32 v0, 6, v0
	v_lshl_or_b32 v6, s2, 2, v0
	v_ashrrev_i32_e32 v7, 31, v6
	v_lshlrev_b64 v[2:3], 11, v[6:7]
	v_mov_b32_e32 v1, 0
	s_waitcnt lgkmcnt(0)
	v_lshl_add_u64 v[8:9], s[4:5], 0, v[2:3]
	v_lshlrev_b32_e32 v4, 3, v12
	v_mov_b32_e32 v5, v1
	v_lshl_add_u64 v[8:9], v[8:9], 0, v[4:5]
	s_mov_b64 s[2:3], 0x400000
	v_lshl_add_u64 v[10:11], v[8:9], 0, s[2:3]
	s_mov_b32 s2, 0x400000
	global_load_dwordx2 v[16:17], v[8:9], off
	global_load_dwordx2 v[18:19], v[8:9], off offset:512
	global_load_dwordx2 v[20:21], v[8:9], off offset:1024
	global_load_dwordx2 v[22:23], v[8:9], off offset:1536
	v_add_co_u32_e32 v8, vcc, s2, v8
	global_load_dwordx2 v[24:25], v[10:11], off offset:512
	global_load_dwordx2 v[26:27], v[10:11], off offset:1024
	global_load_dwordx2 v[28:29], v[10:11], off offset:1536
	v_addc_co_u32_e32 v9, vcc, 0, v9, vcc
	global_load_dwordx2 v[30:31], v[8:9], off
	v_lshlrev_b64 v[6:7], 12, v[6:7]
	v_lshlrev_b32_e32 v0, 4, v12
	v_lshl_add_u64 v[6:7], s[8:9], 0, v[6:7]
	v_lshl_add_u64 v[6:7], v[6:7], 0, v[0:1]
	global_load_dwordx4 v[8:11], v[6:7], off offset:1024
	global_load_dwordx4 v[12:15], v0, s[6:7] offset:1024
	global_load_dwordx4 v[64:67], v[6:7], off
	global_load_dwordx4 v[68:71], v[6:7], off offset:2048
	global_load_dwordx4 v[72:75], v[6:7], off offset:3072
	global_load_dwordx4 v[76:79], v0, s[6:7] offset:2048
	global_load_dwordx4 v[80:83], v0, s[6:7]
	global_load_dwordx4 v[84:87], v0, s[6:7] offset:3072
	global_load_dwordx4 v[96:99], v62, s[12:13]
	global_load_dwordx4 v[100:103], v62, s[12:13] offset:1024
	global_load_dwordx4 v[104:107], v62, s[12:13] offset:2048
	global_load_dwordx4 v[108:111], v62, s[12:13] offset:3072
	global_load_dwordx4 v[112:115], v62, s[14:15]
	global_load_dwordx4 v[116:119], v62, s[14:15] offset:1024
	global_load_dwordx4 v[120:123], v62, s[14:15] offset:2048
	global_load_dwordx4 v[124:127], v62, s[14:15] offset:3072
	s_waitcnt vmcnt(23)
	v_cvt_f32_f16_e32 v32, v16
	s_waitcnt vmcnt(22)
	v_cvt_f32_f16_e32 v36, v18
	v_cvt_f32_f16_sdwa v37, v18 dst_sel:DWORD dst_unused:UNUSED_PAD src0_sel:WORD_1
	v_cvt_f32_f16_e32 v38, v19
	v_cvt_f32_f16_sdwa v39, v19 dst_sel:DWORD dst_unused:UNUSED_PAD src0_sel:WORD_1
	s_waitcnt vmcnt(21)
	v_cvt_f32_f16_e32 v40, v20
	v_cvt_f32_f16_sdwa v41, v20 dst_sel:DWORD dst_unused:UNUSED_PAD src0_sel:WORD_1
	v_cvt_f32_f16_e32 v42, v21
	v_cvt_f32_f16_sdwa v43, v21 dst_sel:DWORD dst_unused:UNUSED_PAD src0_sel:WORD_1
	s_waitcnt vmcnt(20)
	v_cvt_f32_f16_e32 v44, v22
	v_cvt_f32_f16_sdwa v45, v22 dst_sel:DWORD dst_unused:UNUSED_PAD src0_sel:WORD_1
	v_cvt_f32_f16_e32 v46, v23
	v_cvt_f32_f16_sdwa v47, v23 dst_sel:DWORD dst_unused:UNUSED_PAD src0_sel:WORD_1
	s_waitcnt vmcnt(19)
	v_cvt_f32_f16_e32 v20, v24
	v_cvt_f32_f16_sdwa v21, v24 dst_sel:DWORD dst_unused:UNUSED_PAD src0_sel:WORD_1
	v_cvt_f32_f16_e32 v22, v25
	v_cvt_f32_f16_sdwa v23, v25 dst_sel:DWORD dst_unused:UNUSED_PAD src0_sel:WORD_1
	s_waitcnt vmcnt(18)
	v_cvt_f32_f16_e32 v24, v26
	v_cvt_f32_f16_sdwa v25, v26 dst_sel:DWORD dst_unused:UNUSED_PAD src0_sel:WORD_1
	v_cvt_f32_f16_e32 v26, v27
	v_cvt_f32_f16_sdwa v27, v27 dst_sel:DWORD dst_unused:UNUSED_PAD src0_sel:WORD_1
	s_waitcnt vmcnt(17)
	v_cvt_f32_f16_e32 v48, v28
	v_cvt_f32_f16_sdwa v49, v28 dst_sel:DWORD dst_unused:UNUSED_PAD src0_sel:WORD_1
	v_cvt_f32_f16_e32 v28, v29
	v_cvt_f32_f16_sdwa v29, v29 dst_sel:DWORD dst_unused:UNUSED_PAD src0_sel:WORD_1
	v_cvt_f32_f16_sdwa v33, v16 dst_sel:DWORD dst_unused:UNUSED_PAD src0_sel:WORD_1
	v_cvt_f32_f16_e32 v34, v17
	v_cvt_f32_f16_sdwa v35, v17 dst_sel:DWORD dst_unused:UNUSED_PAD src0_sel:WORD_1
	s_waitcnt vmcnt(16)
	v_cvt_f32_f16_e32 v50, v30
	v_cvt_f32_f16_sdwa v51, v30 dst_sel:DWORD dst_unused:UNUSED_PAD src0_sel:WORD_1
	v_cvt_f32_f16_e32 v52, v31
	v_cvt_f32_f16_sdwa v53, v31 dst_sel:DWORD dst_unused:UNUSED_PAD src0_sel:WORD_1
	s_waitcnt vmcnt(8)
	v_mov_b32_e32 v16, v64
	v_mov_b32_e32 v17, v65
	v_mov_b32_e32 v18, v66
	v_mov_b32_e32 v19, v67
	v_pk_add_f32 v[36:37], v[36:37], v[20:21]
	v_pk_add_f32 v[38:39], v[38:39], v[22:23]
	v_mov_b32_e32 v20, v68
	v_mov_b32_e32 v21, v69
	v_mov_b32_e32 v22, v70
	v_mov_b32_e32 v23, v71
	v_pk_add_f32 v[40:41], v[40:41], v[24:25]
	v_pk_add_f32 v[42:43], v[42:43], v[26:27]
	v_mov_b32_e32 v24, v72
	v_mov_b32_e32 v25, v73
	v_mov_b32_e32 v26, v74
	v_mov_b32_e32 v27, v75
	v_pk_add_f32 v[46:47], v[46:47], v[28:29]
	v_mov_b32_e32 v28, v76
	v_mov_b32_e32 v29, v77
	v_mov_b32_e32 v30, v78
	v_mov_b32_e32 v31, v79
	s_waitcnt vmcnt(13)
	v_pk_add_f32 v[36:37], v[8:9], v[36:37]
	v_pk_add_f32 v[38:39], v[10:11], v[38:39]
	v_mov_b32_e32 v8, v80
	v_mov_b32_e32 v9, v81
	v_mov_b32_e32 v10, v82
	v_mov_b32_e32 v11, v83
	v_pk_add_f32 v[44:45], v[44:45], v[48:49]
	v_pk_add_f32 v[48:49], v[32:33], v[50:51]
	v_pk_add_f32 v[50:51], v[34:35], v[52:53]
	v_mov_b32_e32 v32, v84
	v_mov_b32_e32 v33, v85
	v_mov_b32_e32 v34, v86
	v_mov_b32_e32 v35, v87
	s_waitcnt vmcnt(14)
	v_pk_add_f32 v[12:13], v[12:13], v[36:37]
	v_pk_add_f32 v[14:15], v[14:15], v[38:39]
	s_load_dwordx4 s[4:7], s[0:1], 0x28
	s_mov_b32 s0, 0xf800000
	s_waitcnt lgkmcnt(0)
	v_lshl_add_u64 v[2:3], s[6:7], 0, v[2:3]
	s_waitcnt vmcnt(12)
	v_pk_add_f32 v[20:21], v[20:21], v[40:41]
	v_pk_add_f32 v[22:23], v[22:23], v[42:43]
	v_pk_add_f32 v[40:41], v[16:17], v[48:49]
	v_pk_add_f32 v[42:43], v[18:19], v[50:51]
	s_waitcnt vmcnt(11)
	v_pk_add_f32 v[24:25], v[24:25], v[44:45]
	v_pk_add_f32 v[26:27], v[26:27], v[46:47]
	s_waitcnt vmcnt(10)
	v_pk_add_f32 v[16:17], v[28:29], v[20:21]
	v_pk_add_f32 v[18:19], v[30:31], v[22:23]
	s_waitcnt vmcnt(9)
	v_pk_add_f32 v[8:9], v[8:9], v[40:41]
	v_pk_add_f32 v[10:11], v[10:11], v[42:43]
	v_mov_b32_e32 v28, v13
	v_mov_b32_e32 v29, v15
	s_waitcnt vmcnt(8)
	v_pk_add_f32 v[20:21], v[32:33], v[24:25]
	v_pk_add_f32 v[22:23], v[34:35], v[26:27]
	v_mov_b32_e32 v24, v8
	v_mov_b32_e32 v25, v10
	v_mov_b32_e32 v26, v9
	v_mov_b32_e32 v27, v11
	v_pk_add_f32 v[24:25], v[24:25], v[26:27]
	v_mov_b32_e32 v26, v12
	v_mov_b32_e32 v27, v14
	v_pk_add_f32 v[26:27], v[26:27], v[28:29]
	v_add_f32_e32 v1, v24, v25
	v_pk_add_f32 v[26:27], v[26:27], v[26:27] op_sel:[0,1] op_sel_hi:[1,0]
	v_pk_add_f32 v[28:29], v[16:17], v[16:17] op_sel:[0,1] op_sel_hi:[1,0]
	v_pk_add_f32 v[30:31], v[18:19], v[18:19] op_sel:[0,1] op_sel_hi:[1,0]
	v_add_f32_e32 v24, 0, v1
	v_mov_b32_e32 v25, v20
	v_mov_b32_e32 v27, v21
	v_mov_b32_e32 v29, v22
	v_mov_b32_e32 v31, v23
	v_pk_add_f32 v[24:25], v[24:25], v[26:27]
	v_pk_add_f32 v[26:27], v[28:29], v[30:31]
	s_nop 0
	v_pk_add_f32 v[24:25], v[24:25], v[26:27]
	s_nop 0
	v_add_f32_e32 v1, v24, v25
	v_mbcnt_lo_u32_b32 v24, -1, 0
	v_mbcnt_hi_u32_b32 v24, -1, v24
	v_and_b32_e32 v25, 64, v24
	v_add_u32_e32 v25, 64, v25
	v_xor_b32_e32 v26, 32, v24
	v_cmp_lt_i32_e32 vcc, v26, v25
	s_nop 1
	v_cndmask_b32_e32 v26, v24, v26, vcc
	v_lshlrev_b32_e32 v52, 2, v26
	v_mov_b32_e32 v26, v1
	s_waitcnt lgkmcnt(0)
	s_nop 1
	v_permlane32_swap_b32_e32 v1, v26
	v_add_f32_e32 v1, v1, v26
	v_xor_b32_e32 v26, 16, v24
	v_cmp_lt_i32_e32 vcc, v26, v25
	s_nop 1
	v_cndmask_b32_e32 v26, v24, v26, vcc
	v_lshlrev_b32_e32 v53, 2, v26
	v_mov_b32_e32 v26, v1
	s_waitcnt lgkmcnt(0)
	s_nop 1
	v_permlane16_swap_b32_e32 v1, v26
	v_add_f32_e32 v1, v1, v26
	v_xor_b32_e32 v26, 8, v24
	v_cmp_lt_i32_e32 vcc, v26, v25
	s_nop 1
	v_cndmask_b32_e32 v26, v24, v26, vcc
	v_lshlrev_b32_e32 v54, 2, v26
	s_waitcnt lgkmcnt(0)
	s_nop 1
	v_add_f32_dpp v1, v1, v1 row_ror:8 row_mask:0xf bank_mask:0xf
	v_xor_b32_e32 v26, 4, v24
	v_cmp_lt_i32_e32 vcc, v26, v25
	s_nop 1
	v_cndmask_b32_e32 v26, v24, v26, vcc
	v_lshlrev_b32_e32 v55, 2, v26
	s_waitcnt lgkmcnt(0)
	s_nop 1
	v_add_f32_dpp v1, v1, v1 row_ror:4 row_mask:0xf bank_mask:0xf
	v_xor_b32_e32 v26, 2, v24
	v_cmp_lt_i32_e32 vcc, v26, v25
	s_nop 1
	v_cndmask_b32_e32 v26, v24, v26, vcc
	v_lshlrev_b32_e32 v56, 2, v26
	s_waitcnt lgkmcnt(0)
	s_nop 1
	v_add_f32_dpp v1, v1, v1 row_ror:2 row_mask:0xf bank_mask:0xf
	v_xor_b32_e32 v26, 1, v24
	v_cmp_lt_i32_e32 vcc, v26, v25
	s_nop 1
	v_cndmask_b32_e32 v24, v24, v26, vcc
	v_lshlrev_b32_e32 v57, 2, v24
	s_waitcnt lgkmcnt(0)
	s_nop 1
	v_add_f32_dpp v1, v1, v1 row_ror:1 row_mask:0xf bank_mask:0xf
	v_mul_f32_e32 v24, 0x3a800000, v1
	v_pk_add_f32 v[36:37], v[8:9], v[24:25] op_sel_hi:[1,0] neg_lo:[0,1] neg_hi:[0,1]
	v_pk_add_f32 v[38:39], v[10:11], v[24:25] op_sel_hi:[1,0] neg_lo:[0,1] neg_hi:[0,1]
	v_mov_b32_e32 v28, v37
	v_mov_b32_e32 v29, v39
	v_pk_add_f32 v[40:41], v[12:13], v[24:25] op_sel_hi:[1,0] neg_lo:[0,1] neg_hi:[0,1]
	v_pk_add_f32 v[42:43], v[14:15], v[24:25] op_sel_hi:[1,0] neg_lo:[0,1] neg_hi:[0,1]
	v_mov_b32_e32 v26, v36
	v_mov_b32_e32 v27, v38
	v_pk_mul_f32 v[28:29], v[28:29], v[28:29]
	v_mov_b32_e32 v30, v41
	v_mov_b32_e32 v31, v43
	v_pk_fma_f32 v[26:27], v[26:27], v[26:27], v[28:29]
	v_mov_b32_e32 v28, v40
	v_mov_b32_e32 v29, v42
	v_pk_mul_f32 v[30:31], v[30:31], v[30:31]
	v_pk_add_f32 v[44:45], v[16:17], v[24:25] op_sel_hi:[1,0] neg_lo:[0,1] neg_hi:[0,1]
	v_pk_fma_f32 v[28:29], v[28:29], v[28:29], v[30:31]
	v_mul_f32_e32 v30, v44, v44
	v_pk_fma_f32 v[30:31], v[44:45], v[44:45], v[30:31] op_sel_hi:[1,1,0]
	v_pk_add_f32 v[46:47], v[18:19], v[24:25] op_sel_hi:[1,0] neg_lo:[0,1] neg_hi:[0,1]
	v_pk_add_f32 v[48:49], v[20:21], v[24:25] op_sel_hi:[1,0] neg_lo:[0,1] neg_hi:[0,1]
	v_mul_f32_e32 v30, v46, v46
	v_pk_add_f32 v[50:51], v[22:23], v[24:25] op_sel_hi:[1,0] neg_lo:[0,1] neg_hi:[0,1]
	v_pk_fma_f32 v[32:33], v[46:47], v[46:47], v[30:31] op_sel_hi:[1,1,0]
	v_pk_mul_f32 v[34:35], v[48:49], v[48:49]
	v_pk_add_f32 v[26:27], v[26:27], v[26:27] op_sel_hi:[0,1]
	v_pk_add_f32 v[28:29], v[28:29], v[28:29] op_sel_hi:[0,1]
	v_pk_mul_f32 v[24:25], v[50:51], v[50:51]
	v_mov_b32_e32 v30, v34
	v_mov_b32_e32 v32, v35
	v_mov_b32_e32 v26, v24
	v_mov_b32_e32 v28, v25
	v_pk_add_f32 v[30:31], v[30:31], v[32:33]
	v_pk_add_f32 v[24:25], v[26:27], v[28:29]
	s_nop 0
	v_pk_add_f32 v[24:25], v[30:31], v[24:25]
	s_nop 0
	v_add_f32_e32 v1, v24, v25
	v_mov_b32_e32 v24, v1
	s_waitcnt lgkmcnt(0)
	s_nop 1
	v_permlane32_swap_b32_e32 v1, v24
	v_add_f32_e32 v1, v1, v24
	v_mov_b32_e32 v24, v1
	s_waitcnt lgkmcnt(0)
	s_nop 1
	v_permlane16_swap_b32_e32 v1, v24
	v_add_f32_e32 v1, v1, v24
	s_waitcnt lgkmcnt(0)
	s_nop 1
	v_add_f32_dpp v1, v1, v1 row_ror:8 row_mask:0xf bank_mask:0xf
	s_waitcnt lgkmcnt(0)
	s_nop 1
	v_add_f32_dpp v1, v1, v1 row_ror:4 row_mask:0xf bank_mask:0xf
	s_waitcnt vmcnt(0)
	v_mov_b32_e32 v24, v96
	v_mov_b32_e32 v25, v97
	v_mov_b32_e32 v26, v98
	v_mov_b32_e32 v27, v99
	v_mov_b32_e32 v28, v100
	v_mov_b32_e32 v29, v101
	v_mov_b32_e32 v30, v102
	v_mov_b32_e32 v31, v103
	s_waitcnt lgkmcnt(0)
	s_nop 1
	v_add_f32_dpp v1, v1, v1 row_ror:2 row_mask:0xf bank_mask:0xf
	global_store_dwordx4 v[6:7], v[8:11], off
	global_store_dwordx4 v[6:7], v[12:15], off offset:1024
	global_store_dwordx4 v[6:7], v[16:19], off offset:2048
	global_store_dwordx4 v[6:7], v[20:23], off offset:3072
	s_waitcnt lgkmcnt(0)
	s_nop 1
	v_add_f32_dpp v1, v1, v1 row_ror:1 row_mask:0xf bank_mask:0xf
	v_mov_b32_e32 v32, 0x3727c5ac
	v_fmac_f32_e32 v32, 0x3a800000, v1
	v_mul_f32_e32 v1, 0x4f800000, v32
	v_cmp_gt_f32_e32 vcc, s0, v32
	v_mov_b32_e32 v12, v112
	v_mov_b32_e32 v13, v113
	v_mov_b32_e32 v14, v114
	v_mov_b32_e32 v15, v115
	v_mov_b32_e32 v16, v116
	v_mov_b32_e32 v17, v117
	v_mov_b32_e32 v18, v118
	v_mov_b32_e32 v19, v119
	v_cndmask_b32_e32 v1, v32, v1, vcc
	v_sqrt_f32_e32 v32, v1
	v_mov_b32_e32 v8, v104
	v_mov_b32_e32 v9, v105
	v_mov_b32_e32 v10, v106
	v_mov_b32_e32 v11, v107
	v_add_u32_e32 v6, -1, v32
	v_fma_f32 v7, -v6, v32, v1
	v_cmp_ge_f32_e64 s[0:1], 0, v7
	v_add_u32_e32 v7, 1, v32
	v_fma_f32 v20, -v7, v32, v1
	v_cndmask_b32_e64 v6, v32, v6, s[0:1]
	v_cmp_lt_f32_e64 s[0:1], 0, v20
	v_mov_b32_e32 v20, v120
	v_mov_b32_e32 v21, v121
	v_mov_b32_e32 v22, v122
	v_mov_b32_e32 v23, v123
	s_nop 0
	v_cndmask_b32_e64 v6, v6, v7, s[0:1]
	v_mul_f32_e32 v7, 0x37800000, v6
	v_cndmask_b32_e32 v6, v6, v7, vcc
	v_mov_b32_e32 v7, 0x260
	v_cmp_class_f32_e32 vcc, v1, v7
	s_nop 1
	v_cndmask_b32_e32 v1, v6, v1, vcc
	v_div_scale_f32 v32, s[0:1], v1, v1, 1.0
	v_rcp_f32_e32 v33, v32
	v_lshl_add_u64 v[6:7], v[2:3], 0, v[4:5]
	v_div_scale_f32 v34, vcc, 1.0, v1, 1.0
	v_fma_f32 v2, -v32, v33, 1.0
	v_fmac_f32_e32 v33, v2, v33
	v_mul_f32_e32 v35, v34, v33
	v_fma_f32 v2, -v32, v35, v34
	v_fmac_f32_e32 v35, v2, v33
	v_fma_f32 v32, -v32, v35, v34
	v_mov_b32_e32 v2, v108
	v_mov_b32_e32 v3, v109
	v_mov_b32_e32 v4, v110
	v_mov_b32_e32 v5, v111
	v_div_fmas_f32 v52, v32, v33, v35
	v_mov_b32_e32 v32, v124
	v_mov_b32_e32 v33, v125
	v_mov_b32_e32 v34, v126
	v_mov_b32_e32 v35, v127
	v_div_fixup_f32 v0, v52, v1, 1.0
	v_pk_mul_f32 v[36:37], v[36:37], v[0:1] op_sel_hi:[1,0]
	s_waitcnt vmcnt(5)
	v_pk_fma_f32 v[12:13], v[24:25], v[36:37], v[12:13]
	v_pk_mul_f32 v[24:25], v[38:39], v[0:1] op_sel_hi:[1,0]
	v_cvt_pk_f16_f32 v12, v12, v13
	v_pk_fma_f32 v[14:15], v[26:27], v[24:25], v[14:15]
	s_nop 0
	v_cvt_pk_f16_f32 v13, v14, v15
	global_store_dwordx2 v[6:7], v[12:13], off
	v_pk_mul_f32 v[12:13], v[40:41], v[0:1] op_sel_hi:[1,0]
	v_pk_mul_f32 v[14:15], v[42:43], v[0:1] op_sel_hi:[1,0]
	s_waitcnt vmcnt(5)
	v_pk_fma_f32 v[12:13], v[28:29], v[12:13], v[16:17]
	v_pk_fma_f32 v[14:15], v[30:31], v[14:15], v[18:19]
	v_cvt_pk_f16_f32 v12, v12, v13
	v_cvt_pk_f16_f32 v13, v14, v15
	global_store_dwordx2 v[6:7], v[12:13], off offset:512
	v_pk_mul_f32 v[12:13], v[44:45], v[0:1] op_sel_hi:[1,0]
	s_waitcnt vmcnt(4)
	v_pk_fma_f32 v[8:9], v[12:13], v[8:9], v[20:21]
	v_pk_mul_f32 v[12:13], v[46:47], v[0:1] op_sel_hi:[1,0]
	v_cvt_pk_f16_f32 v8, v8, v9
	v_pk_fma_f32 v[10:11], v[12:13], v[10:11], v[22:23]
	s_nop 0
	v_cvt_pk_f16_f32 v9, v10, v11
	global_store_dwordx2 v[6:7], v[8:9], off offset:1024
	v_pk_mul_f32 v[8:9], v[48:49], v[0:1] op_sel_hi:[1,0]
	v_pk_mul_f32 v[0:1], v[50:51], v[0:1] op_sel_hi:[1,0]
	s_waitcnt vmcnt(3)
	v_pk_fma_f32 v[2:3], v[8:9], v[2:3], v[32:33]
	v_pk_fma_f32 v[0:1], v[0:1], v[4:5], v[34:35]
	v_cvt_pk_f16_f32 v2, v2, v3
	v_cvt_pk_f16_f32 v3, v0, v1
	global_store_dwordx2 v[6:7], v[2:3], off offset:1536
	s_endpgm
	s_endpgm
	s_endpgm
	s_endpgm
	s_endpgm
	s_endpgm
	s_endpgm
	s_endpgm
	s_endpgm
	s_endpgm
	s_endpgm
	s_endpgm

	.amdhsa_kernel _Z9ln_kernelILi2EEvPKiPKfS3_PfS3_S3_PDF16_
		.amdhsa_group_segment_fixed_size 0
		.amdhsa_private_segment_fixed_size 0
		.amdhsa_kernarg_size 56
		.amdhsa_user_sgpr_count 2
		.amdhsa_user_sgpr_dispatch_ptr 0
		.amdhsa_user_sgpr_queue_ptr 0
		.amdhsa_user_sgpr_kernarg_segment_ptr 1
		.amdhsa_user_sgpr_dispatch_id 0
		.amdhsa_user_sgpr_kernarg_preload_length 0
		.amdhsa_user_sgpr_kernarg_preload_offset 0
		.amdhsa_user_sgpr_private_segment_size 0
		.amdhsa_uses_dynamic_stack 0
		.amdhsa_enable_private_segment 0
		.amdhsa_system_sgpr_workgroup_id_x 1
		.amdhsa_system_sgpr_workgroup_id_y 0
		.amdhsa_system_sgpr_workgroup_id_z 0
		.amdhsa_system_sgpr_workgroup_info 0
		.amdhsa_system_vgpr_workitem_id 0
		.amdhsa_next_free_vgpr 128
		.amdhsa_next_free_sgpr 16
		.amdhsa_accum_offset 128
		.amdhsa_reserve_vcc 1
		.amdhsa_float_round_mode_32 0
		.amdhsa_float_round_mode_16_64 0
		.amdhsa_float_denorm_mode_32 3
		.amdhsa_float_denorm_mode_16_64 3
		.amdhsa_dx10_clamp 1
		.amdhsa_ieee_mode 1
		.amdhsa_fp16_overflow 0
		.amdhsa_tg_split 0
		.amdhsa_exception_fp_ieee_invalid_op 0
		.amdhsa_exception_fp_denorm_src 0
		.amdhsa_exception_fp_ieee_div_zero 0
		.amdhsa_exception_fp_ieee_overflow 0
		.amdhsa_exception_fp_ieee_underflow 0
		.amdhsa_exception_fp_ieee_inexact 0
		.amdhsa_exception_int_div_zero 0
	.end_amdhsa_kernel

_Z9ln_kernelILi0EEvPKiPKfS3_PfS3_S3_PDF16_:
	s_load_dwordx4 s[12:15], s[0:1], 0x20
	v_and_b32_e32 v62, 63, v0
	v_lshlrev_b32_e32 v62, 4, v62
	s_load_dwordx8 s[4:11], s[0:1], 0x18
	v_and_b32_e32 v52, 63, v0
	v_lshrrev_b32_e32 v0, 6, v0
	v_lshl_or_b32 v0, s2, 2, v0
	v_ashrrev_i32_e32 v1, 31, v0
	v_lshlrev_b64 v[2:3], 12, v[0:1]
	s_waitcnt lgkmcnt(0)
	v_lshl_add_u64 v[4:5], s[4:5], 0, v[2:3]
	v_lshlrev_b32_e32 v2, 4, v52
	v_mov_b32_e32 v3, 0
	v_lshl_add_u64 v[20:21], v[4:5], 0, v[2:3]
	global_load_dwordx4 v[4:7], v[20:21], off offset:1024
	global_load_dwordx4 v[8:11], v[20:21], off offset:2048
	global_load_dwordx4 v[12:15], v[20:21], off
	global_load_dwordx4 v[16:19], v[20:21], off offset:3072
	global_load_dwordx4 v[64:67], v62, s[12:13]
	global_load_dwordx4 v[68:71], v62, s[12:13] offset:1024
	global_load_dwordx4 v[72:75], v62, s[12:13] offset:2048
	global_load_dwordx4 v[76:79], v62, s[12:13] offset:3072
	global_load_dwordx4 v[80:83], v62, s[14:15]
	global_load_dwordx4 v[84:87], v62, s[14:15] offset:1024
	global_load_dwordx4 v[88:91], v62, s[14:15] offset:2048
	global_load_dwordx4 v[92:95], v62, s[14:15] offset:3072
	v_mbcnt_lo_u32_b32 v20, -1, 0
	v_mbcnt_hi_u32_b32 v32, -1, v20
	v_and_b32_e32 v20, 64, v32
	v_xor_b32_e32 v21, 32, v32
	v_add_u32_e32 v34, 64, v20
	v_cmp_lt_i32_e32 vcc, v21, v34
	v_xor_b32_e32 v33, 16, v32
	s_mov_b32 s0, 0xf800000
	v_cndmask_b32_e32 v20, v32, v21, vcc
	v_lshlrev_b32_e32 v53, 2, v20
	v_cmp_lt_i32_e32 vcc, v33, v34
	v_lshlrev_b64 v[0:1], 11, v[0:1]
	v_lshl_add_u64 v[0:1], s[10:11], 0, v[0:1]
	s_waitcnt vmcnt(11)
	v_mov_b32_e32 v36, v5
	v_mov_b32_e32 v37, v6
	v_mov_b32_e32 v5, v7
	s_waitcnt vmcnt(9)
	v_mov_b32_e32 v22, v12
	v_mov_b32_e32 v23, v14
	v_mov_b32_e32 v24, v13
	v_mov_b32_e32 v25, v15
	v_mov_b32_e32 v6, v9
	v_mov_b32_e32 v20, v11
	s_waitcnt vmcnt(8)
	v_mov_b32_e32 v21, v16
	v_pk_add_f32 v[26:27], v[36:37], v[4:5]
	v_pk_add_f32 v[22:23], v[22:23], v[24:25]
	v_pk_add_f32 v[28:29], v[8:9], v[6:7]
	v_pk_add_f32 v[30:31], v[10:11], v[20:21]
	v_pk_add_f32 v[24:25], v[26:27], v[26:27] op_sel:[0,1] op_sel_hi:[1,0]
	v_add_f32_e32 v5, v22, v23
	v_mov_b32_e32 v29, v18
	v_mov_b32_e32 v31, v19
	v_add_f32_e32 v20, 0, v5
	v_mov_b32_e32 v25, v17
	v_pk_add_f32 v[22:23], v[28:29], v[30:31]
	v_pk_add_f32 v[20:21], v[20:21], v[24:25]
	v_pk_mov_b32 v[36:37], v[36:37], v[36:37] op_sel:[1,0]
	v_pk_add_f32 v[20:21], v[20:21], v[22:23]
	s_nop 0
	v_add_f32_e32 v5, v20, v21
	v_mov_b32_e32 v6, v5
	v_cndmask_b32_e32 v21, v32, v33, vcc
	v_lshlrev_b32_e32 v54, 2, v21
	v_xor_b32_e32 v20, 8, v32
	v_cmp_lt_i32_e32 vcc, v20, v34
	s_waitcnt lgkmcnt(0)
	s_nop 1
	v_permlane32_swap_b32_e32 v5, v6
	v_add_f32_e32 v5, v5, v6
	v_mov_b32_e32 v6, v5
	v_cndmask_b32_e32 v20, v32, v20, vcc
	v_lshlrev_b32_e32 v55, 2, v20
	v_xor_b32_e32 v21, 4, v32
	v_cmp_lt_i32_e32 vcc, v21, v34
	s_waitcnt lgkmcnt(0)
	s_nop 1
	v_permlane16_swap_b32_e32 v5, v6
	v_add_f32_e32 v5, v5, v6
	v_cndmask_b32_e32 v21, v32, v21, vcc
	v_lshlrev_b32_e32 v56, 2, v21
	v_xor_b32_e32 v20, 2, v32
	v_cmp_lt_i32_e32 vcc, v20, v34
	s_waitcnt lgkmcnt(0)
	s_nop 1
	v_add_f32_dpp v5, v5, v5 row_ror:8 row_mask:0xf bank_mask:0xf
	v_cndmask_b32_e32 v20, v32, v20, vcc
	v_lshlrev_b32_e32 v57, 2, v20
	v_xor_b32_e32 v21, 1, v32
	v_cmp_lt_i32_e32 vcc, v21, v34
	s_waitcnt lgkmcnt(0)
	s_nop 1
	v_add_f32_dpp v5, v5, v5 row_ror:4 row_mask:0xf bank_mask:0xf
	v_cndmask_b32_e32 v20, v32, v21, vcc
	v_lshlrev_b32_e32 v58, 2, v20
	s_waitcnt vmcnt(0)
	v_mov_b32_e32 v20, v64
	v_mov_b32_e32 v21, v65
	v_mov_b32_e32 v22, v66
	v_mov_b32_e32 v23, v67
	v_mov_b32_e32 v24, v80
	v_mov_b32_e32 v25, v81
	v_mov_b32_e32 v26, v82
	v_mov_b32_e32 v27, v83
	v_mov_b32_e32 v28, v68
	v_mov_b32_e32 v29, v69
	v_mov_b32_e32 v30, v70
	v_mov_b32_e32 v31, v71
	v_mov_b32_e32 v32, v84
	v_mov_b32_e32 v33, v85
	v_mov_b32_e32 v34, v86
	v_mov_b32_e32 v35, v87
	s_waitcnt lgkmcnt(0)
	s_nop 1
	v_add_f32_dpp v6, v5, v5 row_ror:2 row_mask:0xf bank_mask:0xf
	v_mov_b32_e32 v5, v37
	v_mov_b32_e32 v37, v7
	s_waitcnt lgkmcnt(0)
	s_nop 1
	v_add_f32_dpp v6, v6, v6 row_ror:1 row_mask:0xf bank_mask:0xf
	v_mul_f32_e32 v6, 0x3a800000, v6
	v_pk_add_f32 v[38:39], v[12:13], v[6:7] op_sel_hi:[1,0] neg_lo:[0,1] neg_hi:[0,1]
	v_pk_add_f32 v[40:41], v[14:15], v[6:7] op_sel_hi:[1,0] neg_lo:[0,1] neg_hi:[0,1]
	v_pk_add_f32 v[46:47], v[4:5], v[6:7] op_sel_hi:[1,0] neg_lo:[0,1] neg_hi:[0,1]
	v_pk_add_f32 v[36:37], v[36:37], v[6:7] op_sel_hi:[1,0] neg_lo:[0,1] neg_hi:[0,1]
	v_pk_add_f32 v[42:43], v[16:17], v[6:7] op_sel_hi:[1,0] neg_lo:[0,1] neg_hi:[0,1]
	v_pk_add_f32 v[44:45], v[18:19], v[6:7] op_sel_hi:[1,0] neg_lo:[0,1] neg_hi:[0,1]
	v_pk_add_f32 v[48:49], v[8:9], v[6:7] op_sel_hi:[1,0] neg_lo:[0,1] neg_hi:[0,1]
	v_pk_add_f32 v[50:51], v[10:11], v[6:7] op_sel_hi:[1,0] neg_lo:[0,1] neg_hi:[0,1]
	v_mov_b32_e32 v6, v39
	v_mov_b32_e32 v7, v41
	v_mov_b32_e32 v14, v47
	v_mov_b32_e32 v15, v37
	v_mov_b32_e32 v4, v38
	v_mov_b32_e32 v5, v40
	v_mov_b32_e32 v12, v46
	v_mov_b32_e32 v13, v36
	v_pk_mul_f32 v[6:7], v[6:7], v[6:7]
	v_pk_mul_f32 v[14:15], v[14:15], v[14:15]
	v_mul_f32_e32 v16, v48, v48
	v_mul_f32_e32 v18, v50, v50
	v_pk_fma_f32 v[4:5], v[4:5], v[4:5], v[6:7]
	v_pk_fma_f32 v[6:7], v[12:13], v[12:13], v[14:15]
	v_pk_mul_f32 v[8:9], v[42:43], v[42:43]
	v_pk_mul_f32 v[10:11], v[44:45], v[44:45]
	v_pk_fma_f32 v[16:17], v[48:49], v[48:49], v[16:17] op_sel_hi:[1,1,0]
	v_pk_fma_f32 v[18:19], v[50:51], v[50:51], v[18:19] op_sel_hi:[1,1,0]
	v_pk_add_f32 v[4:5], v[4:5], v[4:5] op_sel_hi:[0,1]
	v_pk_add_f32 v[6:7], v[6:7], v[6:7] op_sel_hi:[0,1]
	v_mov_b32_e32 v16, v8
	v_mov_b32_e32 v18, v9
	v_mov_b32_e32 v4, v10
	v_mov_b32_e32 v6, v11
	v_pk_add_f32 v[8:9], v[16:17], v[18:19]
	v_pk_add_f32 v[4:5], v[4:5], v[6:7]
	s_nop 0
	v_pk_add_f32 v[4:5], v[8:9], v[4:5]
	s_nop 0
	v_add_f32_e32 v59, v4, v5
	v_mov_b32_e32 v4, v72
	v_mov_b32_e32 v5, v73
	v_mov_b32_e32 v6, v74
	v_mov_b32_e32 v7, v75
	v_mov_b32_e32 v8, v88
	v_mov_b32_e32 v9, v89
	v_mov_b32_e32 v10, v90
	v_mov_b32_e32 v11, v91
	v_mov_b32_e32 v12, v76
	v_mov_b32_e32 v13, v77
	v_mov_b32_e32 v14, v78
	v_mov_b32_e32 v15, v79
	v_mov_b32_e32 v16, v92
	v_mov_b32_e32 v17, v93
	v_mov_b32_e32 v18, v94
	v_mov_b32_e32 v19, v95
	v_mov_b32_e32 v53, v59
	s_waitcnt lgkmcnt(0)
	s_nop 1
	v_permlane32_swap_b32_e32 v59, v53
	v_add_f32_e32 v2, v59, v53
	v_mov_b32_e32 v53, v2
	v_mov_b32_e32 v54, 0x3727c5ac
	s_waitcnt lgkmcnt(0)
	s_nop 1
	v_permlane16_swap_b32_e32 v2, v53
	v_add_f32_e32 v2, v2, v53
	v_mov_b32_e32 v55, 0x260
	s_waitcnt lgkmcnt(0)
	s_nop 1
	v_add_f32_dpp v2, v2, v2 row_ror:8 row_mask:0xf bank_mask:0xf
	s_waitcnt lgkmcnt(0)
	s_nop 1
	v_add_f32_dpp v2, v2, v2 row_ror:4 row_mask:0xf bank_mask:0xf
	s_waitcnt lgkmcnt(0)
	s_nop 1
	v_add_f32_dpp v2, v2, v2 row_ror:2 row_mask:0xf bank_mask:0xf
	s_waitcnt lgkmcnt(0)
	s_nop 1
	v_add_f32_dpp v2, v2, v2 row_ror:1 row_mask:0xf bank_mask:0xf
	v_fmac_f32_e32 v54, 0x3a800000, v2
	v_mul_f32_e32 v2, 0x4f800000, v54
	v_cmp_gt_f32_e32 vcc, s0, v54
	s_nop 1
	v_cndmask_b32_e32 v53, v54, v2, vcc
	v_sqrt_f32_e32 v54, v53
	v_lshlrev_b32_e32 v2, 3, v52
	v_lshl_add_u64 v[0:1], v[0:1], 0, v[2:3]
	v_add_u32_e32 v52, -1, v54
	v_add_u32_e32 v56, 1, v54
	v_fma_f32 v57, -v52, v54, v53
	v_fma_f32 v58, -v56, v54, v53
	v_cmp_ge_f32_e64 s[0:1], 0, v57
	s_nop 1
	v_cndmask_b32_e64 v52, v54, v52, s[0:1]
	v_cmp_lt_f32_e64 s[0:1], 0, v58
	s_nop 1
	v_cndmask_b32_e64 v52, v52, v56, s[0:1]
	v_mul_f32_e32 v54, 0x37800000, v52
	v_cndmask_b32_e32 v52, v52, v54, vcc
	v_cmp_class_f32_e32 vcc, v53, v55
	s_nop 1
	v_cndmask_b32_e32 v52, v52, v53, vcc
	v_div_scale_f32 v53, s[0:1], v52, v52, 1.0
	v_rcp_f32_e32 v54, v53
	v_div_scale_f32 v2, vcc, 1.0, v52, 1.0
	v_fma_f32 v3, -v53, v54, 1.0
	v_fmac_f32_e32 v54, v3, v54
	v_mul_f32_e32 v3, v2, v54
	v_fma_f32 v55, -v53, v3, v2
	v_fmac_f32_e32 v3, v55, v54
	v_fma_f32 v2, -v53, v3, v2
	v_div_fmas_f32 v2, v2, v54, v3
	v_div_fixup_f32 v2, v2, v52, 1.0
	v_pk_mul_f32 v[38:39], v[38:39], v[2:3] op_sel_hi:[1,0]
	v_pk_mul_f32 v[40:41], v[40:41], v[2:3] op_sel_hi:[1,0]
	v_pk_mul_f32 v[46:47], v[46:47], v[2:3] op_sel_hi:[1,0]
	v_pk_mul_f32 v[36:37], v[36:37], v[2:3] op_sel_hi:[1,0]
	v_pk_mul_f32 v[48:49], v[48:49], v[2:3] op_sel_hi:[1,0]
	v_pk_mul_f32 v[50:51], v[50:51], v[2:3] op_sel_hi:[1,0]
	v_pk_mul_f32 v[42:43], v[42:43], v[2:3] op_sel_hi:[1,0]
	v_pk_mul_f32 v[2:3], v[44:45], v[2:3] op_sel_hi:[1,0]
	s_waitcnt vmcnt(6)
	v_pk_fma_f32 v[20:21], v[20:21], v[38:39], v[24:25]
	v_pk_fma_f32 v[22:23], v[22:23], v[40:41], v[26:27]
	s_waitcnt vmcnt(4)
	v_pk_fma_f32 v[24:25], v[28:29], v[46:47], v[32:33]
	v_pk_fma_f32 v[26:27], v[30:31], v[36:37], v[34:35]
	s_waitcnt vmcnt(2)
	v_pk_fma_f32 v[4:5], v[48:49], v[4:5], v[8:9]
	v_pk_fma_f32 v[6:7], v[50:51], v[6:7], v[10:11]
	s_waitcnt vmcnt(0)
	v_pk_fma_f32 v[8:9], v[42:43], v[12:13], v[16:17]
	v_pk_fma_f32 v[2:3], v[2:3], v[14:15], v[18:19]
	v_cvt_pk_f16_f32 v10, v20, v21
	v_cvt_pk_f16_f32 v11, v22, v23
	v_cvt_pk_f16_f32 v12, v24, v25
	v_cvt_pk_f16_f32 v13, v26, v27
	v_cvt_pk_f16_f32 v4, v4, v5
	v_cvt_pk_f16_f32 v5, v6, v7
	v_cvt_pk_f16_f32 v6, v8, v9
	v_cvt_pk_f16_f32 v7, v2, v3
	global_store_dwordx2 v[0:1], v[10:11], off
	global_store_dwordx2 v[0:1], v[12:13], off offset:512
	global_store_dwordx2 v[0:1], v[4:5], off offset:1024
	global_store_dwordx2 v[0:1], v[6:7], off offset:1536
	s_endpgm
	s_endpgm
	s_endpgm

amdhsa.kernels:
  - .agpr_count:     0
    .args:
      - .offset:         0
        .size:           400
        .value_kind:     by_value
    .group_segment_fixed_size: 33280
    .kernarg_segment_align: 8
    .kernarg_segment_size: 400
    .language:       OpenCL C
    .language_version:
      - 2
      - 0
    .max_flat_workgroup_size: 256
    .name:           _Z10wt_convert7CvtJobs
    .private_segment_fixed_size: 0
    .sgpr_count:     54
    .sgpr_spill_count: 0
    .symbol:         _Z10wt_convert7CvtJobs.kd
    .uniform_work_group_size: 1
    .uses_dynamic_stack: false
    .vgpr_count:     45
    .vgpr_spill_count: 0
    .wavefront_size: 64
  - .agpr_count:     0
    .args:
      - .actual_access:  read_only
        .address_space:  global
        .offset:         0
        .size:           8
        .value_kind:     global_buffer
      - .actual_access:  read_only
        .address_space:  global
        .offset:         8
        .size:           8
        .value_kind:     global_buffer
      - .actual_access:  read_only
        .address_space:  global
        .offset:         16
        .size:           8
        .value_kind:     global_buffer
      - .actual_access:  write_only
        .address_space:  global
        .offset:         24
        .size:           8
        .value_kind:     global_buffer
      - .actual_access:  read_only
        .address_space:  global
        .offset:         32
        .size:           8
        .value_kind:     global_buffer
      - .actual_access:  read_only
        .address_space:  global
        .offset:         40
        .size:           8
        .value_kind:     global_buffer
      - .actual_access:  write_only
        .address_space:  global
        .offset:         48
        .size:           8
        .value_kind:     global_buffer
      - .offset:         56
        .size:           400
        .value_kind:     by_value
    .group_segment_fixed_size: 33280
    .kernarg_segment_align: 8
    .kernarg_segment_size: 456
    .language:       OpenCL C
    .language_version:
      - 2
      - 0
    .max_flat_workgroup_size: 256
    .name:           _Z13embed_ln_convPKiPKfS2_PfS2_S2_PDF16_7CvtJobs
    .private_segment_fixed_size: 0
    .sgpr_count:     36
    .sgpr_spill_count: 0
    .symbol:         _Z13embed_ln_convPKiPKfS2_PfS2_S2_PDF16_7CvtJobs.kd
    .uniform_work_group_size: 1
    .uses_dynamic_stack: false
    .vgpr_count:     79
    .vgpr_spill_count: 0
    .wavefront_size: 64
  - .agpr_count:     0
    .args:
      - .address_space:  global
        .offset:         0
        .size:           8
        .value_kind:     global_buffer
      - .address_space:  global
        .offset:         8
        .size:           8
        .value_kind:     global_buffer
      - .actual_access:  write_only
        .address_space:  global
        .offset:         16
        .size:           8
        .value_kind:     global_buffer
      - .actual_access:  read_only
        .address_space:  global
        .offset:         24
        .size:           8
        .value_kind:     global_buffer
      - .offset:         32
        .size:           4
        .value_kind:     by_value
      - .offset:         36
        .size:           4
        .value_kind:     by_value
      - .offset:         40
        .size:           4
        .value_kind:     by_value
    .group_segment_fixed_size: 0
    .kernarg_segment_align: 8
    .kernarg_segment_size: 44
    .language:       OpenCL C
    .language_version:
      - 2
      - 0
    .max_flat_workgroup_size: 512
    .name:           _Z17gemm_256sq_8phasePKDF16_S0_PfPKfiii
    .private_segment_fixed_size: 0
    .sgpr_count:     47
    .sgpr_spill_count: 0
    .symbol:         _Z17gemm_256sq_8phasePKDF16_S0_PfPKfiii.kd
    .uniform_work_group_size: 1
    .uses_dynamic_stack: false
    .vgpr_count:     244
    .vgpr_spill_count: 0
    .wavefront_size: 64
  - .agpr_count:     0
    .args:
      - .actual_access:  read_only
        .address_space:  global
        .offset:         0
        .size:           8
        .value_kind:     global_buffer
      - .actual_access:  read_only
        .address_space:  global
        .offset:         8
        .size:           8
        .value_kind:     global_buffer
      - .actual_access:  read_only
        .address_space:  global
        .offset:         16
        .size:           8
        .value_kind:     global_buffer
      - .actual_access:  write_only
        .address_space:  global
        .offset:         24
        .size:           8
        .value_kind:     global_buffer
      - .offset:         32
        .size:           400
        .value_kind:     by_value
    .group_segment_fixed_size: 33280
    .kernarg_segment_align: 8
    .kernarg_segment_size: 432
    .language:       OpenCL C
    .language_version:
      - 2
      - 0
    .max_flat_workgroup_size: 256
    .name:           _Z11attn_kernelPKDF16_S0_S0_PDF16_7CvtJobs
    .private_segment_fixed_size: 0
    .sgpr_count:     36
    .sgpr_spill_count: 0
    .symbol:         _Z11attn_kernelPKDF16_S0_S0_PDF16_7CvtJobs.kd
    .uniform_work_group_size: 1
    .uses_dynamic_stack: false
    .vgpr_count:     116
    .vgpr_spill_count: 0
    .wavefront_size: 64
  - .agpr_count:     0
    .args:
      - .address_space:  global
        .offset:         0
        .size:           8
        .value_kind:     global_buffer
      - .address_space:  global
        .offset:         8
        .size:           8
        .value_kind:     global_buffer
      - .offset:         16
        .size:           4
        .value_kind:     by_value
      - .offset:         20
        .size:           4
        .value_kind:     by_value
      - .offset:         24
        .size:           4
        .value_kind:     by_value
      - .actual_access:  write_only
        .address_space:  global
        .offset:         32
        .size:           8
        .value_kind:     global_buffer
      - .actual_access:  read_only
        .address_space:  global
        .offset:         40
        .size:           8
        .value_kind:     global_buffer
      - .actual_access:  read_only
        .address_space:  global
        .offset:         48
        .size:           8
        .value_kind:     global_buffer
      - .offset:         56
        .size:           4
        .value_kind:     hidden_block_count_x
      - .offset:         60
        .size:           4
        .value_kind:     hidden_block_count_y
      - .offset:         64
        .size:           4
        .value_kind:     hidden_block_count_z
      - .offset:         68
        .size:           2
        .value_kind:     hidden_group_size_x
      - .offset:         70
        .size:           2
        .value_kind:     hidden_group_size_y
      - .offset:         72
        .size:           2
        .value_kind:     hidden_group_size_z
      - .offset:         74
        .size:           2
        .value_kind:     hidden_remainder_x
      - .offset:         76
        .size:           2
        .value_kind:     hidden_remainder_y
      - .offset:         78
        .size:           2
        .value_kind:     hidden_remainder_z
      - .offset:         96
        .size:           8
        .value_kind:     hidden_global_offset_x
      - .offset:         104
        .size:           8
        .value_kind:     hidden_global_offset_y
      - .offset:         112
        .size:           8
        .value_kind:     hidden_global_offset_z
      - .offset:         120
        .size:           2
        .value_kind:     hidden_grid_dims
      - .offset:         176
        .size:           4
        .value_kind:     hidden_dynamic_lds_size
    .group_segment_fixed_size: 0
    .kernarg_segment_align: 8
    .kernarg_segment_size: 312
    .language:       OpenCL C
    .language_version:
      - 2
      - 0
    .max_flat_workgroup_size: 512
    .name:           _Z5gemm8ILi192ELi2ELi3ELi0ELi1ELi16EEvPKDF16_S1_iiiPDF16_PfPKf
    .private_segment_fixed_size: 0
    .sgpr_count:     34
    .sgpr_spill_count: 0
    .symbol:         _Z5gemm8ILi192ELi2ELi3ELi0ELi1ELi16EEvPKDF16_S1_iiiPDF16_PfPKf.kd
    .uniform_work_group_size: 1
    .uses_dynamic_stack: false
    .vgpr_count:     125
    .vgpr_spill_count: 0
    .wavefront_size: 64
  - .agpr_count:     0
    .args:
      - .address_space:  global
        .offset:         0
        .size:           8
        .value_kind:     global_buffer
      - .address_space:  global
        .offset:         8
        .size:           8
        .value_kind:     global_buffer
      - .offset:         16
        .size:           4
        .value_kind:     by_value
      - .offset:         20
        .size:           4
        .value_kind:     by_value
      - .offset:         24
        .size:           4
        .value_kind:     by_value
      - .actual_access:  write_only
        .address_space:  global
        .offset:         32
        .size:           8
        .value_kind:     global_buffer
      - .actual_access:  read_only
        .address_space:  global
        .offset:         40
        .size:           8
        .value_kind:     global_buffer
      - .actual_access:  read_only
        .address_space:  global
        .offset:         48
        .size:           8
        .value_kind:     global_buffer
      - .offset:         56
        .size:           4
        .value_kind:     hidden_block_count_x
      - .offset:         60
        .size:           4
        .value_kind:     hidden_block_count_y
      - .offset:         64
        .size:           4
        .value_kind:     hidden_block_count_z
      - .offset:         68
        .size:           2
        .value_kind:     hidden_group_size_x
      - .offset:         70
        .size:           2
        .value_kind:     hidden_group_size_y
      - .offset:         72
        .size:           2
        .value_kind:     hidden_group_size_z
      - .offset:         74
        .size:           2
        .value_kind:     hidden_remainder_x
      - .offset:         76
        .size:           2
        .value_kind:     hidden_remainder_y
      - .offset:         78
        .size:           2
        .value_kind:     hidden_remainder_z
      - .offset:         96
        .size:           8
        .value_kind:     hidden_global_offset_x
      - .offset:         104
        .size:           8
        .value_kind:     hidden_global_offset_y
      - .offset:         112
        .size:           8
        .value_kind:     hidden_global_offset_z
      - .offset:         120
        .size:           2
        .value_kind:     hidden_grid_dims
      - .offset:         176
        .size:           4
        .value_kind:     hidden_dynamic_lds_size
    .group_segment_fixed_size: 0
    .kernarg_segment_align: 8
    .kernarg_segment_size: 312
    .language:       OpenCL C
    .language_version:
      - 2
      - 0
    .max_flat_workgroup_size: 512
    .name:           _Z5gemm8ILi128ELi2ELi2ELi2ELi1ELi16EEvPKDF16_S1_iiiPDF16_PfPKf
    .private_segment_fixed_size: 0
    .sgpr_count:     30
    .sgpr_spill_count: 0
    .symbol:         _Z5gemm8ILi128ELi2ELi2ELi2ELi1ELi16EEvPKDF16_S1_iiiPDF16_PfPKf.kd
    .uniform_work_group_size: 1
    .uses_dynamic_stack: false
    .vgpr_count:     90
    .vgpr_spill_count: 0
    .wavefront_size: 64
  - .agpr_count:     0
    .args:
      - .address_space:  global
        .offset:         0
        .size:           8
        .value_kind:     global_buffer
      - .address_space:  global
        .offset:         8
        .size:           8
        .value_kind:     global_buffer
      - .offset:         16
        .size:           4
        .value_kind:     by_value
      - .offset:         20
        .size:           4
        .value_kind:     by_value
      - .offset:         24
        .size:           4
        .value_kind:     by_value
      - .actual_access:  read_only
        .address_space:  global
        .offset:         32
        .size:           8
        .value_kind:     global_buffer
      - .address_space:  global
        .offset:         40
        .size:           8
        .value_kind:     global_buffer
      - .actual_access:  read_only
        .address_space:  global
        .offset:         48
        .size:           8
        .value_kind:     global_buffer
      - .offset:         56
        .size:           4
        .value_kind:     hidden_block_count_x
      - .offset:         60
        .size:           4
        .value_kind:     hidden_block_count_y
      - .offset:         64
        .size:           4
        .value_kind:     hidden_block_count_z
      - .offset:         68
        .size:           2
        .value_kind:     hidden_group_size_x
      - .offset:         70
        .size:           2
        .value_kind:     hidden_group_size_y
      - .offset:         72
        .size:           2
        .value_kind:     hidden_group_size_z
      - .offset:         74
        .size:           2
        .value_kind:     hidden_remainder_x
      - .offset:         76
        .size:           2
        .value_kind:     hidden_remainder_y
      - .offset:         78
        .size:           2
        .value_kind:     hidden_remainder_z
      - .offset:         96
        .size:           8
        .value_kind:     hidden_global_offset_x
      - .offset:         104
        .size:           8
        .value_kind:     hidden_global_offset_y
      - .offset:         112
        .size:           8
        .value_kind:     hidden_global_offset_z
      - .offset:         120
        .size:           2
        .value_kind:     hidden_grid_dims
      - .offset:         176
        .size:           4
        .value_kind:     hidden_dynamic_lds_size
    .group_segment_fixed_size: 0
    .kernarg_segment_align: 8
    .kernarg_segment_size: 312
    .language:       OpenCL C
    .language_version:
      - 2
      - 0
    .max_flat_workgroup_size: 512
    .name:           _Z5gemm8ILi64ELi4ELi6ELi1ELi1ELi16EEvPKDF16_S1_iiiPDF16_PfPKf
    .private_segment_fixed_size: 0
    .sgpr_count:     34
    .sgpr_spill_count: 0
    .symbol:         _Z5gemm8ILi64ELi4ELi6ELi1ELi1ELi16EEvPKDF16_S1_iiiPDF16_PfPKf.kd
    .uniform_work_group_size: 1
    .uses_dynamic_stack: false
    .vgpr_count:     104
    .vgpr_spill_count: 0
    .wavefront_size: 64
  - .agpr_count:     0
    .args:
      - .address_space:  global
        .offset:         0
        .size:           8
        .value_kind:     global_buffer
      - .address_space:  global
        .offset:         8
        .size:           8
        .value_kind:     global_buffer
      - .offset:         16
        .size:           4
        .value_kind:     by_value
      - .offset:         20
        .size:           4
        .value_kind:     by_value
      - .offset:         24
        .size:           4
        .value_kind:     by_value
      - .actual_access:  write_only
        .address_space:  global
        .offset:         32
        .size:           8
        .value_kind:     global_buffer
      - .actual_access:  read_only
        .address_space:  global
        .offset:         40
        .size:           8
        .value_kind:     global_buffer
      - .actual_access:  read_only
        .address_space:  global
        .offset:         48
        .size:           8
        .value_kind:     global_buffer
    .group_segment_fixed_size: 0
    .kernarg_segment_align: 8
    .kernarg_segment_size: 56
    .language:       OpenCL C
    .language_version:
      - 2
      - 0
    .max_flat_workgroup_size: 512
    .name:           _Z5gemm8ILi128ELi2ELi4ELi4ELi2ELi32EEvPKDF16_S1_iiiPDF16_PfPKf
    .private_segment_fixed_size: 0
    .sgpr_count:     38
    .sgpr_spill_count: 0
    .symbol:         _Z5gemm8ILi128ELi2ELi4ELi4ELi2ELi32EEvPKDF16_S1_iiiPDF16_PfPKf.kd
    .uniform_work_group_size: 1
    .uses_dynamic_stack: false
    .vgpr_count:     107
    .vgpr_spill_count: 0
    .wavefront_size: 64
  - .agpr_count:     0
    .args:
      - .actual_access:  read_only
        .address_space:  global
        .offset:         0
        .size:           8
        .value_kind:     global_buffer
      - .actual_access:  read_only
        .address_space:  global
        .offset:         8
        .size:           8
        .value_kind:     global_buffer
      - .actual_access:  read_only
        .address_space:  global
        .offset:         16
        .size:           8
        .value_kind:     global_buffer
      - .address_space:  global
        .offset:         24
        .size:           8
        .value_kind:     global_buffer
      - .actual_access:  read_only
        .address_space:  global
        .offset:         32
        .size:           8
        .value_kind:     global_buffer
      - .actual_access:  read_only
        .address_space:  global
        .offset:         40
        .size:           8
        .value_kind:     global_buffer
      - .actual_access:  write_only
        .address_space:  global
        .offset:         48
        .size:           8
        .value_kind:     global_buffer
    .group_segment_fixed_size: 0
    .kernarg_segment_align: 8
    .kernarg_segment_size: 56
    .language:       OpenCL C
    .language_version:
      - 2
      - 0
    .max_flat_workgroup_size: 256
    .name:           _Z9ln_kernelILi2EEvPKiPKfS3_PfS3_S3_PDF16_
    .private_segment_fixed_size: 0
    .sgpr_count:     22
    .sgpr_spill_count: 0
    .symbol:         _Z9ln_kernelILi2EEvPKiPKfS3_PfS3_S3_PDF16_.kd
    .uniform_work_group_size: 1
    .uses_dynamic_stack: false
    .vgpr_count:     128
    .vgpr_spill_count: 0
    .wavefront_size: 64
  - .agpr_count:     0
    .args:
      - .actual_access:  read_only
        .address_space:  global
        .offset:         0
        .size:           8
        .value_kind:     global_buffer
      - .actual_access:  read_only
        .address_space:  global
        .offset:         8
        .size:           8
        .value_kind:     global_buffer
      - .actual_access:  read_only
        .address_space:  global
        .offset:         16
        .size:           8
        .value_kind:     global_buffer
      - .actual_access:  read_only
        .address_space:  global
        .offset:         24
        .size:           8
        .value_kind:     global_buffer
      - .actual_access:  read_only
        .address_space:  global
        .offset:         32
        .size:           8
        .value_kind:     global_buffer
      - .actual_access:  read_only
        .address_space:  global
        .offset:         40
        .size:           8
        .value_kind:     global_buffer
      - .actual_access:  write_only
        .address_space:  global
        .offset:         48
        .size:           8
        .value_kind:     global_buffer
    .group_segment_fixed_size: 0
    .kernarg_segment_align: 8
    .kernarg_segment_size: 56
    .language:       OpenCL C
    .language_version:
      - 2
      - 0
    .max_flat_workgroup_size: 256
    .name:           _Z9ln_kernelILi0EEvPKiPKfS3_PfS3_S3_PDF16_
    .private_segment_fixed_size: 0
    .sgpr_count:     22
    .sgpr_spill_count: 0
    .symbol:         _Z9ln_kernelILi0EEvPKiPKfS3_PfS3_S3_PDF16_.kd
    .uniform_work_group_size: 1
    .uses_dynamic_stack: false
    .vgpr_count:     96
    .vgpr_spill_count: 0
    .wavefront_size: 64
  - .agpr_count:     0
    .args:
      - .actual_access:  read_only
        .address_space:  global
        .offset:         0
        .size:           8
        .value_kind:     global_buffer
      - .actual_access:  read_only
        .address_space:  global
        .offset:         8
        .size:           8
        .value_kind:     global_buffer
      - .actual_access:  read_only
        .address_space:  global
        .offset:         16
        .size:           8
        .value_kind:     global_buffer
      - .actual_access:  read_only
        .address_space:  global
        .offset:         24
        .size:           8
        .value_kind:     global_buffer
      - .actual_access:  read_only
        .address_space:  global
        .offset:         32
        .size:           8
        .value_kind:     global_buffer
      - .actual_access:  read_only
        .address_space:  global
        .offset:         40
        .size:           8
        .value_kind:     global_buffer
      - .actual_access:  write_only
        .address_space:  global
        .offset:         48
        .size:           8
        .value_kind:     global_buffer
    .group_segment_fixed_size: 0
    .kernarg_segment_align: 8
    .kernarg_segment_size: 56
    .language:       OpenCL C
    .language_version:
      - 2
      - 0
    .max_flat_workgroup_size: 256
    .name:           _Z9ln_kernelILi4EEvPKiPKfS3_PfS3_S3_PDF16_
    .private_segment_fixed_size: 0
    .sgpr_count:     18
    .sgpr_spill_count: 0
    .symbol:         _Z9ln_kernelILi4EEvPKiPKfS3_PfS3_S3_PDF16_.kd
    .uniform_work_group_size: 1
    .uses_dynamic_stack: false
    .vgpr_count:     64
    .vgpr_spill_count: 0
    .wavefront_size: 64
